# v8 plus nt on the P0 modulation-GEMV weight loads (mod_w read once)
# speedup vs baseline: 1.0085x; 1.0085x over previous
.LBB0_22:
	global_load_dwordx4 v[32:35], v[30:31], off nt
	ds_read2st64_b32 v[26:27], v25 offset1:32
	ds_read2st64_b32 v[36:37], v25 offset0:64 offset1:96
	ds_read_b32 v38, v25 offset:32768
	v_add_u32_e32 v3, -1, v3
	v_cmp_eq_u32_e64 s[0:1], 0, v3
	s_waitcnt lgkmcnt(2)
	v_mov_b32_e32 v44, v27
	s_waitcnt lgkmcnt(1)
	v_mov_b32_e32 v46, v37
	v_lshl_add_u64 v[30:31], v[30:31], 0, s[10:11]
	v_add_u32_e32 v24, 32, v24
	v_add_u32_e32 v25, 0x80, v25
	s_or_b64 s[38:39], s[0:1], s[38:39]
	s_waitcnt vmcnt(0)
	v_pk_fma_f32 v[6:7], v[34:35], v[26:27], v[6:7] op_sel_hi:[1,0,1]
	v_pk_fma_f32 v[4:5], v[32:33], v[26:27], v[4:5] op_sel_hi:[1,0,1]
	v_pk_fma_f32 v[10:11], v[34:35], v[44:45], v[10:11] op_sel_hi:[1,0,1]
	v_pk_fma_f32 v[8:9], v[32:33], v[44:45], v[8:9] op_sel_hi:[1,0,1]
	v_pk_fma_f32 v[14:15], v[34:35], v[36:37], v[14:15] op_sel_hi:[1,0,1]
	v_pk_fma_f32 v[12:13], v[32:33], v[36:37], v[12:13] op_sel_hi:[1,0,1]
	v_pk_fma_f32 v[18:19], v[34:35], v[46:47], v[18:19] op_sel_hi:[1,0,1]
	v_pk_fma_f32 v[16:17], v[32:33], v[46:47], v[16:17] op_sel_hi:[1,0,1]
	s_waitcnt lgkmcnt(0)
	v_pk_fma_f32 v[22:23], v[34:35], v[38:39], v[22:23] op_sel_hi:[1,0,1]
	v_pk_fma_f32 v[20:21], v[32:33], v[38:39], v[20:21] op_sel_hi:[1,0,1]
	s_andn2_b64 exec, exec, s[38:39]
	s_cbranch_execnz .LBB0_22
	s_or_b64 exec, exec, s[38:39]
	v_lshlrev_b32_e32 v25, 2, v24

.LBB0_25:
	v_add_co_u32_e64 v36, s[0:1], s31, v30
	global_load_dwordx4 v[24:27], v[30:31], off nt
	s_nop 0
	v_addc_co_u32_e64 v37, s[0:1], 0, v31, s[0:1]
	v_add_co_u32_e64 v38, s[0:1], s34, v30
	ds_read2_b32 v[32:33], v44 offset1:32
	s_nop 0
	v_addc_co_u32_e64 v39, s[0:1], 0, v31, s[0:1]
	v_add_co_u32_e64 v50, s[0:1], s35, v30
	v_add_u32_e32 v45, 0x2000, v44
	s_nop 0
	v_addc_co_u32_e64 v51, s[0:1], 0, v31, s[0:1]
	v_add_co_u32_e64 v54, s[0:1], s42, v30
	ds_read2_b32 v[34:35], v44 offset0:64 offset1:96
	s_nop 0
	v_addc_co_u32_e64 v55, s[0:1], 0, v31, s[0:1]
	v_add_co_u32_e64 v62, s[0:1], s43, v30
	ds_read2_b32 v[76:77], v44 offset0:128 offset1:160
	ds_read2_b32 v[78:79], v44 offset0:192 offset1:224
	v_addc_co_u32_e64 v63, s[0:1], 0, v31, s[0:1]
	v_add_co_u32_e64 v58, s[0:1], s45, v30
	global_load_dwordx4 v[46:49], v[36:37], off nt
	s_nop 0
	global_load_dwordx4 v[36:39], v[38:39], off nt
	s_nop 0
	global_load_dwordx4 v[50:53], v[50:51], off nt
	v_addc_co_u32_e64 v59, s[0:1], 0, v31, s[0:1]
	v_add_u32_e32 v68, 0x4000, v44
	v_add_u32_e32 v75, 0x6000, v44
	v_add_co_u32_e64 v70, s[0:1], s44, v30
	ds_read2_b32 v[80:81], v45 offset1:32
	ds_read2_b32 v[82:83], v68 offset1:32
	ds_read2_b32 v[84:85], v75 offset1:32
	global_load_dwordx4 v[54:57], v[54:55], off nt
	v_add_u32_e32 v110, 0x8000, v44
	v_addc_co_u32_e64 v71, s[0:1], 0, v31, s[0:1]
	ds_read2_b32 v[86:87], v110 offset1:32
	global_load_dwordx4 v[58:61], v[58:59], off nt
	ds_read2_b32 v[88:89], v45 offset0:64 offset1:96
	ds_read2_b32 v[90:91], v68 offset0:64 offset1:96
	ds_read2_b32 v[92:93], v75 offset0:64 offset1:96
	ds_read2_b32 v[94:95], v110 offset0:64 offset1:96
	global_load_dwordx4 v[62:65], v[62:63], off nt
	s_nop 0
	global_load_dwordx4 v[70:73], v[70:71], off nt
	ds_read2_b32 v[96:97], v45 offset0:128 offset1:160
	ds_read2_b32 v[98:99], v68 offset0:128 offset1:160
	ds_read2_b32 v[100:101], v75 offset0:128 offset1:160
	ds_read2_b32 v[102:103], v110 offset0:128 offset1:160
	ds_read2_b32 v[104:105], v45 offset0:192 offset1:224
	ds_read2_b32 v[106:107], v68 offset0:192 offset1:224
	ds_read2_b32 v[108:109], v75 offset0:192 offset1:224
	ds_read2_b32 v[110:111], v110 offset0:192 offset1:224
	s_waitcnt lgkmcnt(14)
	v_mov_b32_e32 v68, v33
	v_mov_b32_e32 v118, v81
	v_mov_b32_e32 v120, v83
	s_waitcnt lgkmcnt(13)
	v_mov_b32_e32 v122, v85
	s_waitcnt lgkmcnt(12)
	v_mov_b32_e32 v124, v87
	v_mov_b32_e32 v112, v35
	s_waitcnt lgkmcnt(11)
	v_mov_b32_e32 v126, v89
	s_waitcnt lgkmcnt(10)
	v_mov_b32_e32 v128, v91
	s_waitcnt lgkmcnt(9)
	v_mov_b32_e32 v130, v93
	s_waitcnt lgkmcnt(8)
	v_mov_b32_e32 v132, v95
	v_mov_b32_e32 v114, v77
	s_waitcnt lgkmcnt(7)
	v_mov_b32_e32 v134, v97
	s_waitcnt lgkmcnt(6)
	v_mov_b32_e32 v136, v99
	s_waitcnt lgkmcnt(5)
	v_mov_b32_e32 v138, v101
	s_waitcnt lgkmcnt(4)
	v_mov_b32_e32 v140, v103
	v_add_u32_e32 v3, 0x100, v3
	v_cmp_lt_u32_e64 s[0:1], s58, v3
	v_mov_b32_e32 v116, v79
	s_waitcnt lgkmcnt(3)
	v_mov_b32_e32 v142, v105
	s_waitcnt lgkmcnt(2)
	v_mov_b32_e32 v144, v107
	s_waitcnt lgkmcnt(1)
	v_mov_b32_e32 v146, v109
	s_waitcnt lgkmcnt(0)
	v_mov_b32_e32 v148, v111
	v_add_u32_e32 v44, 0x400, v44
	v_lshl_add_u64 v[30:31], v[30:31], 0, s[12:13]
	s_or_b64 s[16:17], s[0:1], s[16:17]
	s_waitcnt vmcnt(7)
	v_pk_fma_f32 v[6:7], v[26:27], v[32:33], v[6:7] op_sel_hi:[1,0,1]
	v_pk_fma_f32 v[4:5], v[24:25], v[32:33], v[4:5] op_sel_hi:[1,0,1]
	v_pk_fma_f32 v[10:11], v[26:27], v[80:81], v[10:11] op_sel_hi:[1,0,1]
	v_pk_fma_f32 v[8:9], v[24:25], v[80:81], v[8:9] op_sel_hi:[1,0,1]
	v_pk_fma_f32 v[14:15], v[26:27], v[82:83], v[14:15] op_sel_hi:[1,0,1]
	v_pk_fma_f32 v[12:13], v[24:25], v[82:83], v[12:13] op_sel_hi:[1,0,1]
	v_pk_fma_f32 v[18:19], v[26:27], v[84:85], v[18:19] op_sel_hi:[1,0,1]
	v_pk_fma_f32 v[16:17], v[24:25], v[84:85], v[16:17] op_sel_hi:[1,0,1]
	v_pk_fma_f32 v[22:23], v[26:27], v[86:87], v[22:23] op_sel_hi:[1,0,1]
	v_pk_fma_f32 v[20:21], v[24:25], v[86:87], v[20:21] op_sel_hi:[1,0,1]
	s_waitcnt vmcnt(6)
	v_pk_fma_f32 v[6:7], v[48:49], v[68:69], v[6:7] op_sel_hi:[1,0,1]
	v_pk_fma_f32 v[4:5], v[46:47], v[68:69], v[4:5] op_sel_hi:[1,0,1]
	v_pk_fma_f32 v[10:11], v[48:49], v[118:119], v[10:11] op_sel_hi:[1,0,1]
	v_pk_fma_f32 v[8:9], v[46:47], v[118:119], v[8:9] op_sel_hi:[1,0,1]
	v_pk_fma_f32 v[14:15], v[48:49], v[120:121], v[14:15] op_sel_hi:[1,0,1]
	v_pk_fma_f32 v[12:13], v[46:47], v[120:121], v[12:13] op_sel_hi:[1,0,1]
	v_pk_fma_f32 v[18:19], v[48:49], v[122:123], v[18:19] op_sel_hi:[1,0,1]
	v_pk_fma_f32 v[16:17], v[46:47], v[122:123], v[16:17] op_sel_hi:[1,0,1]
	v_pk_fma_f32 v[22:23], v[48:49], v[124:125], v[22:23] op_sel_hi:[1,0,1]
	v_pk_fma_f32 v[20:21], v[46:47], v[124:125], v[20:21] op_sel_hi:[1,0,1]
	s_waitcnt vmcnt(5)
	v_pk_fma_f32 v[6:7], v[38:39], v[34:35], v[6:7] op_sel_hi:[1,0,1]
	v_pk_fma_f32 v[4:5], v[36:37], v[34:35], v[4:5] op_sel_hi:[1,0,1]
	v_pk_fma_f32 v[10:11], v[38:39], v[88:89], v[10:11] op_sel_hi:[1,0,1]
	v_pk_fma_f32 v[8:9], v[36:37], v[88:89], v[8:9] op_sel_hi:[1,0,1]
	v_pk_fma_f32 v[14:15], v[38:39], v[90:91], v[14:15] op_sel_hi:[1,0,1]
	v_pk_fma_f32 v[12:13], v[36:37], v[90:91], v[12:13] op_sel_hi:[1,0,1]
	v_pk_fma_f32 v[18:19], v[38:39], v[92:93], v[18:19] op_sel_hi:[1,0,1]
	v_pk_fma_f32 v[16:17], v[36:37], v[92:93], v[16:17] op_sel_hi:[1,0,1]
	v_pk_fma_f32 v[22:23], v[38:39], v[94:95], v[22:23] op_sel_hi:[1,0,1]
	v_pk_fma_f32 v[20:21], v[36:37], v[94:95], v[20:21] op_sel_hi:[1,0,1]
	s_waitcnt vmcnt(4)
	v_pk_fma_f32 v[6:7], v[52:53], v[112:113], v[6:7] op_sel_hi:[1,0,1]
	v_pk_fma_f32 v[4:5], v[50:51], v[112:113], v[4:5] op_sel_hi:[1,0,1]
	v_pk_fma_f32 v[10:11], v[52:53], v[126:127], v[10:11] op_sel_hi:[1,0,1]
	v_pk_fma_f32 v[8:9], v[50:51], v[126:127], v[8:9] op_sel_hi:[1,0,1]
	v_pk_fma_f32 v[14:15], v[52:53], v[128:129], v[14:15] op_sel_hi:[1,0,1]
	v_pk_fma_f32 v[12:13], v[50:51], v[128:129], v[12:13] op_sel_hi:[1,0,1]
	v_pk_fma_f32 v[18:19], v[52:53], v[130:131], v[18:19] op_sel_hi:[1,0,1]
	v_pk_fma_f32 v[16:17], v[50:51], v[130:131], v[16:17] op_sel_hi:[1,0,1]
	v_pk_fma_f32 v[22:23], v[52:53], v[132:133], v[22:23] op_sel_hi:[1,0,1]
	v_pk_fma_f32 v[20:21], v[50:51], v[132:133], v[20:21] op_sel_hi:[1,0,1]
	s_waitcnt vmcnt(3)
	v_pk_fma_f32 v[6:7], v[56:57], v[76:77], v[6:7] op_sel_hi:[1,0,1]
	v_pk_fma_f32 v[4:5], v[54:55], v[76:77], v[4:5] op_sel_hi:[1,0,1]
	v_pk_fma_f32 v[10:11], v[56:57], v[96:97], v[10:11] op_sel_hi:[1,0,1]
	v_pk_fma_f32 v[8:9], v[54:55], v[96:97], v[8:9] op_sel_hi:[1,0,1]
	v_pk_fma_f32 v[14:15], v[56:57], v[98:99], v[14:15] op_sel_hi:[1,0,1]
	v_pk_fma_f32 v[12:13], v[54:55], v[98:99], v[12:13] op_sel_hi:[1,0,1]
	v_pk_fma_f32 v[18:19], v[56:57], v[100:101], v[18:19] op_sel_hi:[1,0,1]
	v_pk_fma_f32 v[16:17], v[54:55], v[100:101], v[16:17] op_sel_hi:[1,0,1]
	v_pk_fma_f32 v[22:23], v[56:57], v[102:103], v[22:23] op_sel_hi:[1,0,1]
	v_pk_fma_f32 v[20:21], v[54:55], v[102:103], v[20:21] op_sel_hi:[1,0,1]
	s_waitcnt vmcnt(1)
	v_pk_fma_f32 v[6:7], v[64:65], v[114:115], v[6:7] op_sel_hi:[1,0,1]
	v_pk_fma_f32 v[4:5], v[62:63], v[114:115], v[4:5] op_sel_hi:[1,0,1]
	v_pk_fma_f32 v[10:11], v[64:65], v[134:135], v[10:11] op_sel_hi:[1,0,1]
	v_pk_fma_f32 v[8:9], v[62:63], v[134:135], v[8:9] op_sel_hi:[1,0,1]
	v_pk_fma_f32 v[14:15], v[64:65], v[136:137], v[14:15] op_sel_hi:[1,0,1]
	v_pk_fma_f32 v[12:13], v[62:63], v[136:137], v[12:13] op_sel_hi:[1,0,1]
	v_pk_fma_f32 v[18:19], v[64:65], v[138:139], v[18:19] op_sel_hi:[1,0,1]
	v_pk_fma_f32 v[16:17], v[62:63], v[138:139], v[16:17] op_sel_hi:[1,0,1]
	v_pk_fma_f32 v[22:23], v[64:65], v[140:141], v[22:23] op_sel_hi:[1,0,1]
	v_pk_fma_f32 v[20:21], v[62:63], v[140:141], v[20:21] op_sel_hi:[1,0,1]
	s_waitcnt vmcnt(0)
	v_pk_fma_f32 v[6:7], v[72:73], v[78:79], v[6:7] op_sel_hi:[1,0,1]
	v_pk_fma_f32 v[4:5], v[70:71], v[78:79], v[4:5] op_sel_hi:[1,0,1]
	v_pk_fma_f32 v[10:11], v[72:73], v[104:105], v[10:11] op_sel_hi:[1,0,1]
	v_pk_fma_f32 v[8:9], v[70:71], v[104:105], v[8:9] op_sel_hi:[1,0,1]
	v_pk_fma_f32 v[14:15], v[72:73], v[106:107], v[14:15] op_sel_hi:[1,0,1]
	v_pk_fma_f32 v[12:13], v[70:71], v[106:107], v[12:13] op_sel_hi:[1,0,1]
	v_pk_fma_f32 v[18:19], v[72:73], v[108:109], v[18:19] op_sel_hi:[1,0,1]
	v_pk_fma_f32 v[16:17], v[70:71], v[108:109], v[16:17] op_sel_hi:[1,0,1]
	v_pk_fma_f32 v[22:23], v[72:73], v[110:111], v[22:23] op_sel_hi:[1,0,1]
	v_pk_fma_f32 v[20:21], v[70:71], v[110:111], v[20:21] op_sel_hi:[1,0,1]
	v_pk_fma_f32 v[6:7], v[60:61], v[116:117], v[6:7] op_sel_hi:[1,0,1]
	v_pk_fma_f32 v[4:5], v[58:59], v[116:117], v[4:5] op_sel_hi:[1,0,1]
	v_pk_fma_f32 v[10:11], v[60:61], v[142:143], v[10:11] op_sel_hi:[1,0,1]
	v_pk_fma_f32 v[8:9], v[58:59], v[142:143], v[8:9] op_sel_hi:[1,0,1]
	v_pk_fma_f32 v[14:15], v[60:61], v[144:145], v[14:15] op_sel_hi:[1,0,1]
	v_pk_fma_f32 v[12:13], v[58:59], v[144:145], v[12:13] op_sel_hi:[1,0,1]
	v_pk_fma_f32 v[18:19], v[60:61], v[146:147], v[18:19] op_sel_hi:[1,0,1]
	v_pk_fma_f32 v[16:17], v[58:59], v[146:147], v[16:17] op_sel_hi:[1,0,1]
	v_pk_fma_f32 v[22:23], v[60:61], v[148:149], v[22:23] op_sel_hi:[1,0,1]
	v_pk_fma_f32 v[20:21], v[58:59], v[148:149], v[20:21] op_sel_hi:[1,0,1]
	s_andn2_b64 exec, exec, s[16:17]
	s_cbranch_execnz .LBB0_25
	s_or_b64 exec, exec, s[16:17]
	ds_write_b128 v40, v[4:7] offset:40960
	ds_write_b128 v40, v[8:11] offset:41216
	ds_write_b128 v40, v[12:15] offset:41472
	ds_write_b128 v40, v[16:19] offset:41728
	ds_write_b128 v40, v[20:23] offset:41984
	s_waitcnt lgkmcnt(0)
	s_barrier
	s_and_saveexec_b64 s[0:1], vcc
	s_cbranch_execz .LBB0_19
	v_mov_b32_e32 v3, 0
	s_mov_b32 s15, 0
